# branch GEMM: epilogues of the two wave halves no longer aligned (stagger kept through the epilogue), + SSD load hoists
# speedup vs baseline: 1.0016x; 1.0016x over previous
.LBB0_985:
	s_lshl_b32 s52, s21, 10
	s_lshl_b32 s20, s6, 7
	s_add_i32 s2, s20, s52
	s_ashr_i32 s3, s2, 31
	s_lshl_b32 s7, s49, 10
	s_lshl_b64 s[24:25], s[2:3], 10
	s_lshl_b32 s2, s50, 7
	s_add_i32 s2, s7, s2
	s_ashr_i32 s3, s2, 31
	s_mul_i32 s51, s28, 0x1a0000
	s_lshl_b64 s[2:3], s[2:3], 10
	s_mul_hi_i32 s19, s28, 0x1a0000
	s_add_u32 s6, s8, s51
	s_addc_u32 s19, s9, s19
	s_add_u32 s54, s6, s52
	s_addc_u32 s55, s19, 0
	s_add_u32 s56, s30, s24
	s_addc_u32 s57, s31, s25
	s_add_i32 s52, 0, 0x10000
	v_add_u32_e32 v28, s52, v96
	ds_read_b128 v[30:33], v28
	ds_read_b128 v[34:37], v28 offset:1024
	ds_read_b128 v[38:41], v28 offset:2048
	ds_read_b128 v[42:45], v28 offset:3072
	v_lshl_add_u64 v[16:17], s[54:55], 0, v[86:87]
	s_add_i32 s25, s34, 0xc000
	v_lshl_add_u64 v[18:19], v[16:17], 0, s[84:85]
	s_mov_b32 m0, s25
	ds_read_b128 v[20:23], v97
	ds_read_b128 v[24:27], v97 offset:1024
	ds_read_b128 v[46:49], v97 offset:2048
	ds_read_b128 v[50:53], v97 offset:3072
	ds_read_b128 v[54:57], v97 offset:4096
	ds_read_b128 v[58:61], v97 offset:5120
	ds_read_b128 v[62:65], v97 offset:6144
	ds_read_b128 v[66:69], v97 offset:7168
	global_load_lds_dwordx4 v[18:19], off
	v_lshl_add_u64 v[18:19], s[54:55], 0, v[90:91]
	s_add_i32 s19, s34, 0xe000
	v_lshl_add_u64 v[70:71], v[18:19], 0, s[84:85]
	s_mov_b32 m0, s19
	s_nop 0
	global_load_lds_dwordx4 v[70:71], off
	s_waitcnt vmcnt(6)
	s_waitcnt lgkmcnt(0)
	s_barrier
	s_setprio 1
	s_waitcnt lgkmcnt(0)
	v_mfma_f32_16x16x32_bf16 v[70:73], v[30:33], v[20:23], 0
	v_mfma_f32_16x16x32_bf16 v[20:23], v[38:41], v[20:23], 0
	v_mfma_f32_16x16x32_bf16 v[74:77], v[42:45], v[24:27], v[20:23]
	v_mfma_f32_16x16x32_bf16 v[20:23], v[30:33], v[46:49], 0
	v_mfma_f32_16x16x32_bf16 v[166:169], v[34:37], v[50:53], v[20:23]
	v_mfma_f32_16x16x32_bf16 v[20:23], v[38:41], v[46:49], 0
	v_mfma_f32_16x16x32_bf16 v[46:49], v[42:45], v[50:53], v[20:23]
	v_mfma_f32_16x16x32_bf16 v[20:23], v[30:33], v[54:57], 0
	v_mfma_f32_16x16x32_bf16 v[50:53], v[34:37], v[58:61], v[20:23]
	v_mfma_f32_16x16x32_bf16 v[20:23], v[38:41], v[54:57], 0
	v_mfma_f32_16x16x32_bf16 v[54:57], v[42:45], v[58:61], v[20:23]
	v_mfma_f32_16x16x32_bf16 v[20:23], v[30:33], v[62:65], 0
	v_mfma_f32_16x16x32_bf16 v[58:61], v[34:37], v[66:69], v[20:23]
	v_mfma_f32_16x16x32_bf16 v[20:23], v[38:41], v[62:65], 0
	v_mfma_f32_16x16x32_bf16 v[70:73], v[34:37], v[24:27], v[70:73]
	v_mfma_f32_16x16x32_bf16 v[62:65], v[42:45], v[66:69], v[20:23]
	s_setprio 0
	s_barrier
	s_nop 3
	v_lshl_add_u64 v[20:21], s[56:57], 0, v[80:81]
	s_mov_b64 s[58:59], 0x100
	s_add_i32 s52, s52, s29
	v_lshl_add_u64 v[22:23], v[20:21], 0, s[58:59]
	s_mov_b32 m0, s52
	ds_read_b128 v[66:69], v97 offset:16384
	ds_read_b128 v[170:173], v97 offset:17408
	ds_read_b128 v[174:177], v97 offset:18432
	ds_read_b128 v[178:181], v97 offset:19456
	ds_read_b128 v[182:185], v97 offset:20480
	ds_read_b128 v[186:189], v97 offset:21504
	ds_read_b128 v[190:193], v97 offset:22528
	ds_read_b128 v[194:197], v97 offset:23552
	global_load_lds_dwordx4 v[22:23], off
	v_lshl_add_u64 v[22:23], s[56:57], 0, v[82:83]
	s_add_i32 s24, s52, 0x2000
	v_lshl_add_u64 v[24:25], v[22:23], 0, s[58:59]
	s_mov_b32 m0, s24
	s_nop 0
	global_load_lds_dwordx4 v[24:25], off
	v_lshl_add_u64 v[24:25], s[54:55], 0, v[84:85]
	v_lshl_add_u64 v[26:27], v[24:25], 0, s[58:59]
	s_mov_b32 m0, s34
	s_nop 0
	global_load_lds_dwordx4 v[26:27], off
	v_lshl_add_u64 v[26:27], s[54:55], 0, v[88:89]
	v_lshl_add_u64 v[78:79], v[26:27], 0, s[58:59]
	s_mov_b32 m0, s35
	s_nop 0
	global_load_lds_dwordx4 v[78:79], off
	s_waitcnt vmcnt(6)
	s_waitcnt lgkmcnt(0)
	s_barrier
	s_setprio 1
	s_waitcnt lgkmcnt(0)
	v_mfma_f32_16x16x32_bf16 v[198:201], v[30:33], v[66:69], 0
	v_mfma_f32_16x16x32_bf16 v[66:69], v[38:41], v[66:69], 0
	v_mfma_f32_16x16x32_bf16 v[198:201], v[34:37], v[170:173], v[198:201]
	v_mfma_f32_16x16x32_bf16 v[66:69], v[42:45], v[170:173], v[66:69]
	v_mfma_f32_16x16x32_bf16 v[170:173], v[30:33], v[174:177], 0
	v_mfma_f32_16x16x32_bf16 v[174:177], v[38:41], v[174:177], 0
	v_mfma_f32_16x16x32_bf16 v[170:173], v[34:37], v[178:181], v[170:173]
	v_mfma_f32_16x16x32_bf16 v[174:177], v[42:45], v[178:181], v[174:177]
	v_mfma_f32_16x16x32_bf16 v[178:181], v[30:33], v[182:185], 0
	v_mfma_f32_16x16x32_bf16 v[30:33], v[30:33], v[190:193], 0
	v_mfma_f32_16x16x32_bf16 v[178:181], v[34:37], v[186:189], v[178:181]
	v_mfma_f32_16x16x32_bf16 v[30:33], v[34:37], v[194:197], v[30:33]
	v_mfma_f32_16x16x32_bf16 v[34:37], v[38:41], v[190:193], 0
	v_mfma_f32_16x16x32_bf16 v[182:185], v[38:41], v[182:185], 0
	v_mfma_f32_16x16x32_bf16 v[34:37], v[42:45], v[194:197], v[34:37]
	v_mfma_f32_16x16x32_bf16 v[182:185], v[42:45], v[186:189], v[182:185]
	s_setprio 0
	s_barrier
	s_add_i32 s53, 0, 0x18000
	v_add_u32_e32 v29, s53, v96
	ds_read_b128 v[38:41], v29
	ds_read_b128 v[42:45], v29 offset:1024
	ds_read_b128 v[186:189], v29 offset:2048
	ds_read_b128 v[190:193], v29 offset:3072
	s_mov_b32 m0, s36
	v_lshl_add_u64 v[78:79], v[16:17], 0, s[58:59]
	ds_read_b128 v[194:197], v97 offset:32768
	ds_read_b128 v[202:205], v97 offset:33792
	ds_read_b128 v[210:213], v97 offset:34816
	ds_read_b128 v[214:217], v97 offset:35840
	ds_read_b128 v[218:221], v97 offset:36864
	ds_read_b128 v[226:229], v97 offset:37888
	ds_read_b128 v[232:235], v97 offset:38912
	ds_read_b128 v[236:239], v97 offset:39936
	global_load_lds_dwordx4 v[78:79], off
	v_lshl_add_u64 v[78:79], v[18:19], 0, s[58:59]
	s_mov_b32 m0, s37
	s_nop 0
	global_load_lds_dwordx4 v[78:79], off
	s_waitcnt vmcnt(6)
	s_waitcnt lgkmcnt(0)
	s_barrier
	s_setprio 1
	s_waitcnt lgkmcnt(0)
	v_mfma_f32_16x16x32_bf16 v[70:73], v[38:41], v[194:197], v[70:73]
	v_mfma_f32_16x16x32_bf16 v[74:77], v[186:189], v[194:197], v[74:77]
	v_mfma_f32_16x16x32_bf16 v[46:49], v[186:189], v[210:213], v[46:49]
	v_mfma_f32_16x16x32_bf16 v[50:53], v[38:41], v[218:221], v[50:53]
	v_mfma_f32_16x16x32_bf16 v[54:57], v[186:189], v[218:221], v[54:57]
	v_mfma_f32_16x16x32_bf16 v[58:61], v[38:41], v[232:235], v[58:61]
	v_mfma_f32_16x16x32_bf16 v[62:65], v[186:189], v[232:235], v[62:65]
	v_mfma_f32_16x16x32_bf16 v[70:73], v[42:45], v[202:205], v[70:73]
	v_mfma_f32_16x16x32_bf16 v[74:77], v[190:193], v[202:205], v[74:77]
	v_mfma_f32_16x16x32_bf16 v[166:169], v[38:41], v[210:213], v[166:169]
	v_mfma_f32_16x16x32_bf16 v[46:49], v[190:193], v[214:217], v[46:49]
	v_mfma_f32_16x16x32_bf16 v[50:53], v[42:45], v[226:229], v[50:53]
	v_mfma_f32_16x16x32_bf16 v[54:57], v[190:193], v[226:229], v[54:57]
	v_mfma_f32_16x16x32_bf16 v[58:61], v[42:45], v[236:239], v[58:61]
	v_mfma_f32_16x16x32_bf16 v[62:65], v[190:193], v[236:239], v[62:65]
	v_mfma_f32_16x16x32_bf16 v[166:169], v[42:45], v[214:217], v[166:169]
	s_setprio 0
	s_barrier
	s_mov_b64 s[54:55], 0x180
	s_add_i32 s53, s53, s29
	v_lshl_add_u64 v[78:79], v[20:21], 0, s[54:55]
	s_mov_b32 m0, s53
	s_add_i32 s51, s53, 0x2000
	ds_read_b128 v[194:197], v97 offset:49152
	ds_read_b128 v[202:205], v97 offset:50176
	ds_read_b128 v[210:213], v97 offset:51200
	ds_read_b128 v[214:217], v97 offset:52224
	ds_read_b128 v[218:221], v97 offset:53248
	ds_read_b128 v[226:229], v97 offset:54272
	ds_read_b128 v[232:235], v97 offset:55296
	ds_read_b128 v[236:239], v97 offset:56320
	global_load_lds_dwordx4 v[78:79], off
	v_lshl_add_u64 v[78:79], v[22:23], 0, s[54:55]
	s_mov_b32 m0, s51
	s_nop 0
	global_load_lds_dwordx4 v[78:79], off
	v_lshl_add_u64 v[78:79], v[24:25], 0, s[54:55]
	s_mov_b32 m0, s41
	s_nop 0
	global_load_lds_dwordx4 v[78:79], off
	v_lshl_add_u64 v[78:79], v[26:27], 0, s[54:55]
	s_mov_b32 m0, s42
	s_nop 0
	global_load_lds_dwordx4 v[78:79], off
	s_waitcnt vmcnt(6)
	s_waitcnt lgkmcnt(0)
	s_barrier
	s_setprio 1
	s_waitcnt lgkmcnt(0)
	v_mfma_f32_16x16x32_bf16 v[66:69], v[186:189], v[194:197], v[66:69]
	v_mfma_f32_16x16x32_bf16 v[30:33], v[38:41], v[232:235], v[30:33]
	v_mfma_f32_16x16x32_bf16 v[34:37], v[186:189], v[232:235], v[34:37]
	v_mfma_f32_16x16x32_bf16 v[198:201], v[38:41], v[194:197], v[198:201]
	v_mfma_f32_16x16x32_bf16 v[66:69], v[190:193], v[202:205], v[66:69]
	v_mfma_f32_16x16x32_bf16 v[170:173], v[38:41], v[210:213], v[170:173]
	v_mfma_f32_16x16x32_bf16 v[174:177], v[186:189], v[210:213], v[174:177]
	v_mfma_f32_16x16x32_bf16 v[178:181], v[38:41], v[218:221], v[178:181]
	v_mfma_f32_16x16x32_bf16 v[182:185], v[186:189], v[218:221], v[182:185]
	v_mfma_f32_16x16x32_bf16 v[30:33], v[42:45], v[236:239], v[30:33]
	v_mfma_f32_16x16x32_bf16 v[34:37], v[190:193], v[236:239], v[34:37]
	v_mfma_f32_16x16x32_bf16 v[198:201], v[42:45], v[202:205], v[198:201]
	v_mfma_f32_16x16x32_bf16 v[170:173], v[42:45], v[214:217], v[170:173]
	v_mfma_f32_16x16x32_bf16 v[174:177], v[190:193], v[214:217], v[174:177]
	v_mfma_f32_16x16x32_bf16 v[178:181], v[42:45], v[226:229], v[178:181]
	v_mfma_f32_16x16x32_bf16 v[182:185], v[190:193], v[226:229], v[182:185]
	s_setprio 0
	s_barrier
	ds_read_b128 v[38:41], v28
	ds_read_b128 v[42:45], v28 offset:1024
	ds_read_b128 v[186:189], v28 offset:2048
	ds_read_b128 v[190:193], v28 offset:3072
	s_mov_b32 m0, s25
	v_lshl_add_u64 v[78:79], v[16:17], 0, s[54:55]
	ds_read_b128 v[194:197], v97
	ds_read_b128 v[202:205], v97 offset:1024
	ds_read_b128 v[210:213], v97 offset:2048
	ds_read_b128 v[214:217], v97 offset:3072
	ds_read_b128 v[218:221], v97 offset:4096
	ds_read_b128 v[226:229], v97 offset:5120
	ds_read_b128 v[232:235], v97 offset:6144
	ds_read_b128 v[236:239], v97 offset:7168
	global_load_lds_dwordx4 v[78:79], off
	v_lshl_add_u64 v[78:79], v[18:19], 0, s[54:55]
	s_mov_b32 m0, s19
	s_nop 0
	global_load_lds_dwordx4 v[78:79], off
	s_waitcnt vmcnt(6)
	s_waitcnt lgkmcnt(0)
	s_barrier
	s_setprio 1
	s_waitcnt lgkmcnt(0)
	v_mfma_f32_16x16x32_bf16 v[70:73], v[38:41], v[194:197], v[70:73]
	v_mfma_f32_16x16x32_bf16 v[74:77], v[186:189], v[194:197], v[74:77]
	v_mfma_f32_16x16x32_bf16 v[46:49], v[186:189], v[210:213], v[46:49]
	v_mfma_f32_16x16x32_bf16 v[50:53], v[38:41], v[218:221], v[50:53]
	v_mfma_f32_16x16x32_bf16 v[54:57], v[186:189], v[218:221], v[54:57]
	v_mfma_f32_16x16x32_bf16 v[58:61], v[38:41], v[232:235], v[58:61]
	v_mfma_f32_16x16x32_bf16 v[62:65], v[186:189], v[232:235], v[62:65]
	v_mfma_f32_16x16x32_bf16 v[70:73], v[42:45], v[202:205], v[70:73]
	v_mfma_f32_16x16x32_bf16 v[74:77], v[190:193], v[202:205], v[74:77]
	v_mfma_f32_16x16x32_bf16 v[166:169], v[38:41], v[210:213], v[166:169]
	v_mfma_f32_16x16x32_bf16 v[46:49], v[190:193], v[214:217], v[46:49]
	v_mfma_f32_16x16x32_bf16 v[50:53], v[42:45], v[226:229], v[50:53]
	v_mfma_f32_16x16x32_bf16 v[54:57], v[190:193], v[226:229], v[54:57]
	v_mfma_f32_16x16x32_bf16 v[58:61], v[42:45], v[236:239], v[58:61]
	v_mfma_f32_16x16x32_bf16 v[62:65], v[190:193], v[236:239], v[62:65]
	v_mfma_f32_16x16x32_bf16 v[166:169], v[42:45], v[214:217], v[166:169]
	s_setprio 0
	s_barrier
	s_mov_b64 s[54:55], 0x200
	s_mov_b32 m0, s52
	v_lshl_add_u64 v[78:79], v[20:21], 0, s[54:55]
	ds_read_b128 v[194:197], v97 offset:16384
	ds_read_b128 v[202:205], v97 offset:17408
	ds_read_b128 v[210:213], v97 offset:18432
	ds_read_b128 v[214:217], v97 offset:19456
	ds_read_b128 v[218:221], v97 offset:20480
	ds_read_b128 v[226:229], v97 offset:21504
	ds_read_b128 v[232:235], v97 offset:22528
	ds_read_b128 v[236:239], v97 offset:23552
	global_load_lds_dwordx4 v[78:79], off
	v_lshl_add_u64 v[78:79], v[22:23], 0, s[54:55]
	s_mov_b32 m0, s24
	s_nop 0
	global_load_lds_dwordx4 v[78:79], off
	v_lshl_add_u64 v[78:79], v[24:25], 0, s[54:55]
	s_mov_b32 m0, s34
	s_nop 0
	global_load_lds_dwordx4 v[78:79], off
	v_lshl_add_u64 v[78:79], v[26:27], 0, s[54:55]
	s_mov_b32 m0, s35
	s_nop 0
	global_load_lds_dwordx4 v[78:79], off
	s_waitcnt vmcnt(6)
	s_waitcnt lgkmcnt(0)
	s_barrier
	s_setprio 1
	s_waitcnt lgkmcnt(0)
	v_mfma_f32_16x16x32_bf16 v[66:69], v[186:189], v[194:197], v[66:69]
	v_mfma_f32_16x16x32_bf16 v[30:33], v[38:41], v[232:235], v[30:33]
	v_mfma_f32_16x16x32_bf16 v[34:37], v[186:189], v[232:235], v[34:37]
	v_mfma_f32_16x16x32_bf16 v[198:201], v[38:41], v[194:197], v[198:201]
	v_mfma_f32_16x16x32_bf16 v[66:69], v[190:193], v[202:205], v[66:69]
	v_mfma_f32_16x16x32_bf16 v[170:173], v[38:41], v[210:213], v[170:173]
	v_mfma_f32_16x16x32_bf16 v[174:177], v[186:189], v[210:213], v[174:177]
	v_mfma_f32_16x16x32_bf16 v[178:181], v[38:41], v[218:221], v[178:181]
	v_mfma_f32_16x16x32_bf16 v[182:185], v[186:189], v[218:221], v[182:185]
	v_mfma_f32_16x16x32_bf16 v[30:33], v[42:45], v[236:239], v[30:33]
	v_mfma_f32_16x16x32_bf16 v[34:37], v[190:193], v[236:239], v[34:37]
	v_mfma_f32_16x16x32_bf16 v[198:201], v[42:45], v[202:205], v[198:201]
	v_mfma_f32_16x16x32_bf16 v[170:173], v[42:45], v[214:217], v[170:173]
	v_mfma_f32_16x16x32_bf16 v[174:177], v[190:193], v[214:217], v[174:177]
	v_mfma_f32_16x16x32_bf16 v[178:181], v[42:45], v[226:229], v[178:181]
	v_mfma_f32_16x16x32_bf16 v[182:185], v[190:193], v[226:229], v[182:185]
	s_setprio 0
	s_barrier
	ds_read_b128 v[38:41], v29
	ds_read_b128 v[42:45], v29 offset:1024
	ds_read_b128 v[186:189], v29 offset:2048
	ds_read_b128 v[190:193], v29 offset:3072
	s_mov_b32 m0, s36
	v_lshl_add_u64 v[78:79], v[16:17], 0, s[54:55]
	ds_read_b128 v[194:197], v97 offset:32768
	ds_read_b128 v[202:205], v97 offset:33792
	ds_read_b128 v[210:213], v97 offset:34816
	ds_read_b128 v[214:217], v97 offset:35840
	ds_read_b128 v[218:221], v97 offset:36864
	ds_read_b128 v[226:229], v97 offset:37888
	ds_read_b128 v[232:235], v97 offset:38912
	ds_read_b128 v[236:239], v97 offset:39936
	global_load_lds_dwordx4 v[78:79], off
	v_lshl_add_u64 v[78:79], v[18:19], 0, s[54:55]
	s_mov_b32 m0, s37
	s_nop 0
	global_load_lds_dwordx4 v[78:79], off
	s_waitcnt vmcnt(6)
	s_waitcnt lgkmcnt(0)
	s_barrier
	s_setprio 1
	s_waitcnt lgkmcnt(0)
	v_mfma_f32_16x16x32_bf16 v[70:73], v[38:41], v[194:197], v[70:73]
	v_mfma_f32_16x16x32_bf16 v[74:77], v[186:189], v[194:197], v[74:77]
	v_mfma_f32_16x16x32_bf16 v[46:49], v[186:189], v[210:213], v[46:49]
	v_mfma_f32_16x16x32_bf16 v[50:53], v[38:41], v[218:221], v[50:53]
	v_mfma_f32_16x16x32_bf16 v[54:57], v[186:189], v[218:221], v[54:57]
	v_mfma_f32_16x16x32_bf16 v[58:61], v[38:41], v[232:235], v[58:61]
	v_mfma_f32_16x16x32_bf16 v[62:65], v[186:189], v[232:235], v[62:65]
	v_mfma_f32_16x16x32_bf16 v[70:73], v[42:45], v[202:205], v[70:73]
	v_mfma_f32_16x16x32_bf16 v[74:77], v[190:193], v[202:205], v[74:77]
	v_mfma_f32_16x16x32_bf16 v[166:169], v[38:41], v[210:213], v[166:169]
	v_mfma_f32_16x16x32_bf16 v[46:49], v[190:193], v[214:217], v[46:49]
	v_mfma_f32_16x16x32_bf16 v[50:53], v[42:45], v[226:229], v[50:53]
	v_mfma_f32_16x16x32_bf16 v[54:57], v[190:193], v[226:229], v[54:57]
	v_mfma_f32_16x16x32_bf16 v[58:61], v[42:45], v[236:239], v[58:61]
	v_mfma_f32_16x16x32_bf16 v[62:65], v[190:193], v[236:239], v[62:65]
	v_mfma_f32_16x16x32_bf16 v[166:169], v[42:45], v[214:217], v[166:169]
	s_setprio 0
	s_barrier
	s_mov_b64 s[54:55], 0x280
	s_mov_b32 m0, s53
	v_lshl_add_u64 v[78:79], v[20:21], 0, s[54:55]
	ds_read_b128 v[194:197], v97 offset:49152
	ds_read_b128 v[202:205], v97 offset:50176
	ds_read_b128 v[210:213], v97 offset:51200
	ds_read_b128 v[214:217], v97 offset:52224
	ds_read_b128 v[218:221], v97 offset:53248
	ds_read_b128 v[226:229], v97 offset:54272
	ds_read_b128 v[232:235], v97 offset:55296
	ds_read_b128 v[236:239], v97 offset:56320
	global_load_lds_dwordx4 v[78:79], off
	v_lshl_add_u64 v[78:79], v[22:23], 0, s[54:55]
	s_mov_b32 m0, s51
	s_nop 0
	global_load_lds_dwordx4 v[78:79], off
	v_lshl_add_u64 v[78:79], v[24:25], 0, s[54:55]
	s_mov_b32 m0, s41
	s_nop 0
	global_load_lds_dwordx4 v[78:79], off
	v_lshl_add_u64 v[78:79], v[26:27], 0, s[54:55]
	s_mov_b32 m0, s42
	s_nop 0
	global_load_lds_dwordx4 v[78:79], off
	s_waitcnt vmcnt(6)
	s_waitcnt lgkmcnt(0)
	s_barrier
	s_setprio 1
	s_waitcnt lgkmcnt(0)
	v_mfma_f32_16x16x32_bf16 v[66:69], v[186:189], v[194:197], v[66:69]
	v_mfma_f32_16x16x32_bf16 v[30:33], v[38:41], v[232:235], v[30:33]
	v_mfma_f32_16x16x32_bf16 v[34:37], v[186:189], v[232:235], v[34:37]
	v_mfma_f32_16x16x32_bf16 v[198:201], v[38:41], v[194:197], v[198:201]
	v_mfma_f32_16x16x32_bf16 v[66:69], v[190:193], v[202:205], v[66:69]
	v_mfma_f32_16x16x32_bf16 v[170:173], v[38:41], v[210:213], v[170:173]
	v_mfma_f32_16x16x32_bf16 v[174:177], v[186:189], v[210:213], v[174:177]
	v_mfma_f32_16x16x32_bf16 v[178:181], v[38:41], v[218:221], v[178:181]
	v_mfma_f32_16x16x32_bf16 v[182:185], v[186:189], v[218:221], v[182:185]
	v_mfma_f32_16x16x32_bf16 v[30:33], v[42:45], v[236:239], v[30:33]
	v_mfma_f32_16x16x32_bf16 v[34:37], v[190:193], v[236:239], v[34:37]
	v_mfma_f32_16x16x32_bf16 v[198:201], v[42:45], v[202:205], v[198:201]
	v_mfma_f32_16x16x32_bf16 v[170:173], v[42:45], v[214:217], v[170:173]
	v_mfma_f32_16x16x32_bf16 v[174:177], v[190:193], v[214:217], v[174:177]
	v_mfma_f32_16x16x32_bf16 v[178:181], v[42:45], v[226:229], v[178:181]
	v_mfma_f32_16x16x32_bf16 v[182:185], v[190:193], v[226:229], v[182:185]
	s_setprio 0
	s_barrier
	ds_read_b128 v[38:41], v28
	ds_read_b128 v[42:45], v28 offset:1024
	ds_read_b128 v[186:189], v28 offset:2048
	ds_read_b128 v[190:193], v28 offset:3072
	s_mov_b32 m0, s25
	v_lshl_add_u64 v[78:79], v[16:17], 0, s[54:55]
	ds_read_b128 v[194:197], v97
	ds_read_b128 v[202:205], v97 offset:1024
	ds_read_b128 v[210:213], v97 offset:2048
	ds_read_b128 v[214:217], v97 offset:3072
	ds_read_b128 v[218:221], v97 offset:4096
	ds_read_b128 v[226:229], v97 offset:5120
	ds_read_b128 v[232:235], v97 offset:6144
	ds_read_b128 v[236:239], v97 offset:7168
	global_load_lds_dwordx4 v[78:79], off
	v_lshl_add_u64 v[78:79], v[18:19], 0, s[54:55]
	s_mov_b32 m0, s19
	s_nop 0
	global_load_lds_dwordx4 v[78:79], off
	s_waitcnt vmcnt(6)
	s_waitcnt lgkmcnt(0)
	s_barrier
	s_setprio 1
	s_waitcnt lgkmcnt(0)
	v_mfma_f32_16x16x32_bf16 v[70:73], v[38:41], v[194:197], v[70:73]
	v_mfma_f32_16x16x32_bf16 v[74:77], v[186:189], v[194:197], v[74:77]
	v_mfma_f32_16x16x32_bf16 v[46:49], v[186:189], v[210:213], v[46:49]
	v_mfma_f32_16x16x32_bf16 v[50:53], v[38:41], v[218:221], v[50:53]
	v_mfma_f32_16x16x32_bf16 v[54:57], v[186:189], v[218:221], v[54:57]
	v_mfma_f32_16x16x32_bf16 v[58:61], v[38:41], v[232:235], v[58:61]
	v_mfma_f32_16x16x32_bf16 v[62:65], v[186:189], v[232:235], v[62:65]
	v_mfma_f32_16x16x32_bf16 v[70:73], v[42:45], v[202:205], v[70:73]
	v_mfma_f32_16x16x32_bf16 v[74:77], v[190:193], v[202:205], v[74:77]
	v_mfma_f32_16x16x32_bf16 v[166:169], v[38:41], v[210:213], v[166:169]
	v_mfma_f32_16x16x32_bf16 v[46:49], v[190:193], v[214:217], v[46:49]
	v_mfma_f32_16x16x32_bf16 v[50:53], v[42:45], v[226:229], v[50:53]
	v_mfma_f32_16x16x32_bf16 v[54:57], v[190:193], v[226:229], v[54:57]
	v_mfma_f32_16x16x32_bf16 v[58:61], v[42:45], v[236:239], v[58:61]
	v_mfma_f32_16x16x32_bf16 v[62:65], v[190:193], v[236:239], v[62:65]
	v_mfma_f32_16x16x32_bf16 v[166:169], v[42:45], v[214:217], v[166:169]
	s_setprio 0
	s_barrier
	s_mov_b64 s[54:55], 0x300
	s_mov_b32 m0, s52
	v_lshl_add_u64 v[78:79], v[20:21], 0, s[54:55]
	ds_read_b128 v[194:197], v97 offset:16384
	ds_read_b128 v[202:205], v97 offset:17408
	ds_read_b128 v[210:213], v97 offset:18432
	ds_read_b128 v[214:217], v97 offset:19456
	ds_read_b128 v[218:221], v97 offset:20480
	ds_read_b128 v[226:229], v97 offset:21504
	ds_read_b128 v[232:235], v97 offset:22528
	ds_read_b128 v[236:239], v97 offset:23552
	global_load_lds_dwordx4 v[78:79], off
	v_lshl_add_u64 v[78:79], v[22:23], 0, s[54:55]
	s_mov_b32 m0, s24
	s_nop 0
	global_load_lds_dwordx4 v[78:79], off
	v_lshl_add_u64 v[78:79], v[24:25], 0, s[54:55]
	s_mov_b32 m0, s34
	s_nop 0
	global_load_lds_dwordx4 v[78:79], off
	v_lshl_add_u64 v[78:79], v[26:27], 0, s[54:55]
	s_mov_b32 m0, s35
	s_nop 0
	global_load_lds_dwordx4 v[78:79], off
	s_waitcnt vmcnt(6)
	s_waitcnt lgkmcnt(0)
	s_barrier
	s_setprio 1
	s_waitcnt lgkmcnt(0)
	v_mfma_f32_16x16x32_bf16 v[66:69], v[186:189], v[194:197], v[66:69]
	v_mfma_f32_16x16x32_bf16 v[30:33], v[38:41], v[232:235], v[30:33]
	v_mfma_f32_16x16x32_bf16 v[34:37], v[186:189], v[232:235], v[34:37]
	v_mfma_f32_16x16x32_bf16 v[198:201], v[38:41], v[194:197], v[198:201]
	v_mfma_f32_16x16x32_bf16 v[66:69], v[190:193], v[202:205], v[66:69]
	v_mfma_f32_16x16x32_bf16 v[170:173], v[38:41], v[210:213], v[170:173]
	v_mfma_f32_16x16x32_bf16 v[174:177], v[186:189], v[210:213], v[174:177]
	v_mfma_f32_16x16x32_bf16 v[178:181], v[38:41], v[218:221], v[178:181]
	v_mfma_f32_16x16x32_bf16 v[182:185], v[186:189], v[218:221], v[182:185]
	v_mfma_f32_16x16x32_bf16 v[30:33], v[42:45], v[236:239], v[30:33]
	v_mfma_f32_16x16x32_bf16 v[34:37], v[190:193], v[236:239], v[34:37]
	v_mfma_f32_16x16x32_bf16 v[198:201], v[42:45], v[202:205], v[198:201]
	v_mfma_f32_16x16x32_bf16 v[170:173], v[42:45], v[214:217], v[170:173]
	v_mfma_f32_16x16x32_bf16 v[174:177], v[190:193], v[214:217], v[174:177]
	v_mfma_f32_16x16x32_bf16 v[178:181], v[42:45], v[226:229], v[178:181]
	v_mfma_f32_16x16x32_bf16 v[182:185], v[190:193], v[226:229], v[182:185]
	s_setprio 0
	s_barrier
	ds_read_b128 v[38:41], v29
	ds_read_b128 v[42:45], v29 offset:1024
	ds_read_b128 v[186:189], v29 offset:2048
	ds_read_b128 v[190:193], v29 offset:3072
	s_mov_b32 m0, s36
	v_lshl_add_u64 v[78:79], v[16:17], 0, s[54:55]
	ds_read_b128 v[194:197], v97 offset:32768
	ds_read_b128 v[202:205], v97 offset:33792
	ds_read_b128 v[210:213], v97 offset:34816
	ds_read_b128 v[214:217], v97 offset:35840
	ds_read_b128 v[218:221], v97 offset:36864
	ds_read_b128 v[226:229], v97 offset:37888
	ds_read_b128 v[232:235], v97 offset:38912
	ds_read_b128 v[236:239], v97 offset:39936
	global_load_lds_dwordx4 v[78:79], off
	v_lshl_add_u64 v[78:79], v[18:19], 0, s[54:55]
	s_mov_b32 m0, s37
	s_nop 0
	global_load_lds_dwordx4 v[78:79], off
	s_waitcnt vmcnt(6)
	s_waitcnt lgkmcnt(0)
	s_barrier
	s_setprio 1
	s_waitcnt lgkmcnt(0)
	v_mfma_f32_16x16x32_bf16 v[70:73], v[38:41], v[194:197], v[70:73]
	v_mfma_f32_16x16x32_bf16 v[74:77], v[186:189], v[194:197], v[74:77]
	v_mfma_f32_16x16x32_bf16 v[46:49], v[186:189], v[210:213], v[46:49]
	v_mfma_f32_16x16x32_bf16 v[50:53], v[38:41], v[218:221], v[50:53]
	v_mfma_f32_16x16x32_bf16 v[54:57], v[186:189], v[218:221], v[54:57]
	v_mfma_f32_16x16x32_bf16 v[58:61], v[38:41], v[232:235], v[58:61]
	v_mfma_f32_16x16x32_bf16 v[62:65], v[186:189], v[232:235], v[62:65]
	v_mfma_f32_16x16x32_bf16 v[70:73], v[42:45], v[202:205], v[70:73]
	v_mfma_f32_16x16x32_bf16 v[74:77], v[190:193], v[202:205], v[74:77]
	v_mfma_f32_16x16x32_bf16 v[166:169], v[38:41], v[210:213], v[166:169]
	v_mfma_f32_16x16x32_bf16 v[46:49], v[190:193], v[214:217], v[46:49]
	v_mfma_f32_16x16x32_bf16 v[50:53], v[42:45], v[226:229], v[50:53]
	v_mfma_f32_16x16x32_bf16 v[54:57], v[190:193], v[226:229], v[54:57]
	v_mfma_f32_16x16x32_bf16 v[58:61], v[42:45], v[236:239], v[58:61]
	v_mfma_f32_16x16x32_bf16 v[62:65], v[190:193], v[236:239], v[62:65]
	v_mfma_f32_16x16x32_bf16 v[166:169], v[42:45], v[214:217], v[166:169]
	s_setprio 0
	s_barrier
	s_mov_b64 s[56:57], 0x380
	s_mov_b32 m0, s53
	v_lshl_add_u64 v[20:21], v[20:21], 0, s[56:57]
	ds_read_b128 v[194:197], v97 offset:49152
	ds_read_b128 v[202:205], v97 offset:50176
	ds_read_b128 v[210:213], v97 offset:51200
	ds_read_b128 v[214:217], v97 offset:52224
	ds_read_b128 v[218:221], v97 offset:53248
	ds_read_b128 v[226:229], v97 offset:54272
	ds_read_b128 v[232:235], v97 offset:55296
	ds_read_b128 v[236:239], v97 offset:56320
	global_load_lds_dwordx4 v[20:21], off
	v_lshl_add_u64 v[20:21], v[22:23], 0, s[56:57]
	s_mov_b32 m0, s51
	s_nop 0
	global_load_lds_dwordx4 v[20:21], off
	v_lshl_add_u64 v[20:21], v[24:25], 0, s[56:57]
	s_mov_b32 m0, s41
	s_nop 0
	global_load_lds_dwordx4 v[20:21], off
	v_lshl_add_u64 v[20:21], v[26:27], 0, s[56:57]
	s_mov_b32 m0, s42
	s_nop 0
	global_load_lds_dwordx4 v[20:21], off
	s_waitcnt vmcnt(6)
	s_waitcnt lgkmcnt(0)
	s_barrier
	s_setprio 1
	s_waitcnt lgkmcnt(0)
	v_mfma_f32_16x16x32_bf16 v[20:23], v[38:41], v[194:197], v[198:201]
	v_mfma_f32_16x16x32_bf16 v[24:27], v[186:189], v[194:197], v[66:69]
	v_mfma_f32_16x16x32_bf16 v[66:69], v[38:41], v[210:213], v[170:173]
	v_mfma_f32_16x16x32_bf16 v[30:33], v[38:41], v[232:235], v[30:33]
	v_mfma_f32_16x16x32_bf16 v[34:37], v[186:189], v[232:235], v[34:37]
	v_mfma_f32_16x16x32_bf16 v[20:23], v[42:45], v[202:205], v[20:23]
	v_mfma_f32_16x16x32_bf16 v[24:27], v[190:193], v[202:205], v[24:27]
	v_mfma_f32_16x16x32_bf16 v[66:69], v[42:45], v[214:217], v[66:69]
	v_mfma_f32_16x16x32_bf16 v[170:173], v[186:189], v[210:213], v[174:177]
	v_mfma_f32_16x16x32_bf16 v[174:177], v[38:41], v[218:221], v[178:181]
	v_mfma_f32_16x16x32_bf16 v[178:181], v[186:189], v[218:221], v[182:185]
	v_mfma_f32_16x16x32_bf16 v[30:33], v[42:45], v[236:239], v[30:33]
	v_mfma_f32_16x16x32_bf16 v[34:37], v[190:193], v[236:239], v[34:37]
	v_mfma_f32_16x16x32_bf16 v[170:173], v[190:193], v[214:217], v[170:173]
	v_mfma_f32_16x16x32_bf16 v[174:177], v[42:45], v[226:229], v[174:177]
	v_mfma_f32_16x16x32_bf16 v[178:181], v[190:193], v[226:229], v[178:181]
	s_setprio 0
	s_barrier
	ds_read_b128 v[38:41], v28
	ds_read_b128 v[42:45], v28 offset:1024
	ds_read_b128 v[182:185], v28 offset:2048
	ds_read_b128 v[186:189], v28 offset:3072
	s_mul_i32 s6, s18, 0x1a0000
	s_add_u32 s6, s8, s6
	s_mul_hi_i32 s54, s18, 0x1a0000
	s_addc_u32 s54, s9, s54
	s_add_u32 s6, s6, s7
	s_addc_u32 s7, s54, 0
	s_add_u32 s2, s30, s2
	s_addc_u32 s3, s31, s3
	s_mov_b32 m0, s25
	v_lshl_add_u64 v[16:17], v[16:17], 0, s[56:57]
	ds_read_b128 v[190:193], v97
	ds_read_b128 v[194:197], v97 offset:1024
	ds_read_b128 v[198:201], v97 offset:2048
	ds_read_b128 v[202:205], v97 offset:3072
	ds_read_b128 v[210:213], v97 offset:4096
	ds_read_b128 v[214:217], v97 offset:5120
	ds_read_b128 v[218:221], v97 offset:6144
	ds_read_b128 v[226:229], v97 offset:7168
	global_load_lds_dwordx4 v[16:17], off
	v_lshl_add_u64 v[16:17], v[18:19], 0, s[56:57]
	s_mov_b32 m0, s19
	s_nop 0
	global_load_lds_dwordx4 v[16:17], off
	s_waitcnt vmcnt(6)
	s_waitcnt lgkmcnt(0)
	s_barrier
	s_setprio 1
	s_waitcnt lgkmcnt(0)
	v_mfma_f32_16x16x32_bf16 v[16:19], v[38:41], v[190:193], v[70:73]
	v_mfma_f32_16x16x32_bf16 v[70:73], v[182:185], v[190:193], v[74:77]
	v_mfma_f32_16x16x32_bf16 v[46:49], v[182:185], v[198:201], v[46:49]
	v_mfma_f32_16x16x32_bf16 v[50:53], v[38:41], v[210:213], v[50:53]
	v_mfma_f32_16x16x32_bf16 v[54:57], v[182:185], v[210:213], v[54:57]
	v_mfma_f32_16x16x32_bf16 v[58:61], v[38:41], v[218:221], v[58:61]
	v_mfma_f32_16x16x32_bf16 v[16:19], v[42:45], v[194:197], v[16:19]
	v_mfma_f32_16x16x32_bf16 v[70:73], v[186:189], v[194:197], v[70:73]
	v_mfma_f32_16x16x32_bf16 v[74:77], v[38:41], v[198:201], v[166:169]
	v_mfma_f32_16x16x32_bf16 v[46:49], v[186:189], v[202:205], v[46:49]
	v_mfma_f32_16x16x32_bf16 v[50:53], v[42:45], v[214:217], v[50:53]
	v_mfma_f32_16x16x32_bf16 v[54:57], v[186:189], v[214:217], v[54:57]
	v_mfma_f32_16x16x32_bf16 v[190:193], v[42:45], v[226:229], v[58:61]
	v_mfma_f32_16x16x32_bf16 v[58:61], v[182:185], v[218:221], v[62:65]
	v_mfma_f32_16x16x32_bf16 v[166:169], v[42:45], v[202:205], v[74:77]
	v_mfma_f32_16x16x32_bf16 v[194:197], v[186:189], v[226:229], v[58:61]
	s_setprio 0
	s_barrier
	s_mov_b32 m0, s52
	v_lshl_add_u64 v[206:207], s[2:3], 0, v[80:81]
	s_nop 1
	ds_read_b128 v[58:61], v97 offset:16384
	ds_read_b128 v[62:65], v97 offset:17408
	ds_read_b128 v[74:77], v97 offset:18432
	ds_read_b128 v[198:201], v97 offset:19456
	ds_read_b128 v[202:205], v97 offset:20480
	ds_read_b128 v[210:213], v97 offset:21504
	ds_read_b128 v[214:217], v97 offset:22528
	ds_read_b128 v[218:221], v97 offset:23552
	global_load_lds_dwordx4 v[206:207], off
	v_lshl_add_u64 v[244:245], s[2:3], 0, v[82:83]
	s_mov_b32 m0, s24
	v_lshl_add_u64 v[246:247], s[6:7], 0, v[84:85]
	global_load_lds_dwordx4 v[244:245], off
	s_mov_b32 m0, s34
	v_lshl_add_u64 v[248:249], s[6:7], 0, v[88:89]
	global_load_lds_dwordx4 v[246:247], off
	s_mov_b32 m0, s35
	s_nop 0
	global_load_lds_dwordx4 v[248:249], off
	s_waitcnt vmcnt(6)
	s_waitcnt lgkmcnt(0)
	s_barrier
	s_setprio 1
	s_waitcnt lgkmcnt(0)
	v_mfma_f32_16x16x32_bf16 v[20:23], v[38:41], v[58:61], v[20:23]
	v_mfma_f32_16x16x32_bf16 v[24:27], v[182:185], v[58:61], v[24:27]
	v_mfma_f32_16x16x32_bf16 v[58:61], v[38:41], v[74:77], v[66:69]
	v_mfma_f32_16x16x32_bf16 v[226:229], v[42:45], v[198:201], v[58:61]
	v_mfma_f32_16x16x32_bf16 v[58:61], v[182:185], v[74:77], v[170:173]
	v_mfma_f32_16x16x32_bf16 v[170:173], v[186:189], v[198:201], v[58:61]
	v_mfma_f32_16x16x32_bf16 v[58:61], v[38:41], v[202:205], v[174:177]
	v_mfma_f32_16x16x32_bf16 v[30:33], v[38:41], v[214:217], v[30:33]
	v_mfma_f32_16x16x32_bf16 v[20:23], v[42:45], v[62:65], v[20:23]
	v_mfma_f32_16x16x32_bf16 v[24:27], v[186:189], v[62:65], v[24:27]
	v_mfma_f32_16x16x32_bf16 v[174:177], v[42:45], v[210:213], v[58:61]
	v_mfma_f32_16x16x32_bf16 v[58:61], v[182:185], v[202:205], v[178:181]
	v_mfma_f32_16x16x32_bf16 v[198:201], v[42:45], v[218:221], v[30:33]
	v_mfma_f32_16x16x32_bf16 v[30:33], v[182:185], v[214:217], v[34:37]
	v_mfma_f32_16x16x32_bf16 v[178:181], v[186:189], v[210:213], v[58:61]
	v_mfma_f32_16x16x32_bf16 v[182:185], v[186:189], v[218:221], v[30:33]
	s_setprio 0
	s_barrier
	ds_read_b128 v[186:189], v29
	ds_read_b128 v[202:205], v29 offset:1024
	ds_read_b128 v[210:213], v29 offset:2048
	ds_read_b128 v[214:217], v29 offset:3072
	s_mov_b32 m0, s36
	v_lshl_add_u64 v[44:45], s[6:7], 0, v[86:87]
	ds_read_b128 v[28:31], v97 offset:32768
	ds_read_b128 v[32:35], v97 offset:33792
	ds_read_b128 v[36:39], v97 offset:34816
	ds_read_b128 v[40:43], v97 offset:35840
	ds_read_b128 v[218:221], v97 offset:36864
	ds_read_b128 v[232:235], v97 offset:37888
	ds_read_b128 v[236:239], v97 offset:38912
	ds_read_b128 v[240:243], v97 offset:39936
	global_load_lds_dwordx4 v[44:45], off
	v_lshl_add_u64 v[44:45], s[6:7], 0, v[90:91]
	s_mov_b32 m0, s37
	s_nop 0
	global_load_lds_dwordx4 v[44:45], off
	s_waitcnt vmcnt(6)
	s_waitcnt lgkmcnt(0)
	s_barrier
	s_setprio 1
	s_waitcnt lgkmcnt(0)
	v_mfma_f32_16x16x32_bf16 v[16:19], v[186:189], v[28:31], v[16:19]
	v_mfma_f32_16x16x32_bf16 v[76:79], v[202:205], v[32:35], v[16:19]
	v_mfma_f32_16x16x32_bf16 v[16:19], v[210:213], v[28:31], v[70:73]
	v_mfma_f32_16x16x32_bf16 v[72:75], v[214:217], v[32:35], v[16:19]
	v_mfma_f32_16x16x32_bf16 v[16:19], v[186:189], v[36:39], v[166:169]
	v_mfma_f32_16x16x32_bf16 v[68:71], v[202:205], v[40:43], v[16:19]
	v_mfma_f32_16x16x32_bf16 v[16:19], v[210:213], v[36:39], v[46:49]
	v_mfma_f32_16x16x32_bf16 v[64:67], v[214:217], v[40:43], v[16:19]
	v_mfma_f32_16x16x32_bf16 v[16:19], v[186:189], v[218:221], v[50:53]
	v_mfma_f32_16x16x32_bf16 v[60:63], v[202:205], v[232:235], v[16:19]
	v_mfma_f32_16x16x32_bf16 v[16:19], v[210:213], v[218:221], v[54:57]
	v_mfma_f32_16x16x32_bf16 v[56:59], v[214:217], v[232:235], v[16:19]
	v_mfma_f32_16x16x32_bf16 v[16:19], v[186:189], v[236:239], v[190:193]
	v_mfma_f32_16x16x32_bf16 v[52:55], v[202:205], v[240:243], v[16:19]
	v_mfma_f32_16x16x32_bf16 v[16:19], v[210:213], v[236:239], v[194:197]
	v_mfma_f32_16x16x32_bf16 v[48:51], v[214:217], v[240:243], v[16:19]
	s_setprio 0
	s_barrier
	s_mov_b32 m0, s53
	v_lshl_add_u64 v[36:37], v[206:207], 0, s[84:85]
	s_nop 2
	ds_read_b128 v[16:19], v97 offset:49152
	ds_read_b128 v[28:31], v97 offset:50176
	ds_read_b128 v[32:35], v97 offset:51200
	ds_read_b128 v[166:169], v97 offset:52224
	ds_read_b128 v[190:193], v97 offset:53248
	ds_read_b128 v[194:197], v97 offset:54272
	ds_read_b128 v[218:221], v97 offset:55296
	ds_read_b128 v[232:235], v97 offset:56320
	global_load_lds_dwordx4 v[36:37], off
	v_lshl_add_u64 v[36:37], v[244:245], 0, s[84:85]
	s_mov_b32 m0, s51
	s_nop 0
	global_load_lds_dwordx4 v[36:37], off
	v_lshl_add_u64 v[36:37], v[246:247], 0, s[84:85]
	s_mov_b32 m0, s41
	s_nop 0
	global_load_lds_dwordx4 v[36:37], off
	v_lshl_add_u64 v[36:37], v[248:249], 0, s[84:85]
	s_mov_b32 m0, s42
	s_nop 0
	global_load_lds_dwordx4 v[36:37], off
	s_waitcnt vmcnt(6)
	s_waitcnt lgkmcnt(0)
	s_barrier
	s_setprio 1
	s_waitcnt lgkmcnt(0)
	v_mfma_f32_16x16x32_bf16 v[20:23], v[186:189], v[16:19], v[20:23]
	v_mfma_f32_16x16x32_bf16 v[16:19], v[210:213], v[16:19], v[24:27]
	v_mfma_f32_16x16x32_bf16 v[40:43], v[214:217], v[28:31], v[16:19]
	v_mfma_f32_16x16x32_bf16 v[16:19], v[186:189], v[32:35], v[226:229]
	v_mfma_f32_16x16x32_bf16 v[36:39], v[202:205], v[166:169], v[16:19]
	v_mfma_f32_16x16x32_bf16 v[16:19], v[210:213], v[32:35], v[170:173]
	v_mfma_f32_16x16x32_bf16 v[32:35], v[214:217], v[166:169], v[16:19]
	v_mfma_f32_16x16x32_bf16 v[16:19], v[186:189], v[190:193], v[174:177]
	v_mfma_f32_16x16x32_bf16 v[44:47], v[202:205], v[28:31], v[20:23]
	v_mfma_f32_16x16x32_bf16 v[28:31], v[202:205], v[194:197], v[16:19]
	v_mfma_f32_16x16x32_bf16 v[16:19], v[210:213], v[190:193], v[178:181]
	v_mfma_f32_16x16x32_bf16 v[24:27], v[214:217], v[194:197], v[16:19]
	v_mfma_f32_16x16x32_bf16 v[16:19], v[186:189], v[218:221], v[198:201]
	v_mfma_f32_16x16x32_bf16 v[20:23], v[202:205], v[232:235], v[16:19]
	v_mfma_f32_16x16x32_bf16 v[16:19], v[210:213], v[218:221], v[182:185]
	v_mfma_f32_16x16x32_bf16 v[16:19], v[214:217], v[232:235], v[16:19]
	s_setprio 0
	s_barrier
	s_andn2_b64 vcc, exec, s[12:13]
	s_cbranch_vccnz .LBB0_987
.LBB0_987:
	s_cmp_eq_u32 s21, 2
	v_mov_b32_e32 v173, 1.0
	s_cselect_b64 s[24:25], -1, 0
	s_cmp_lg_u32 s21, 2
	v_mov_b32_e32 v174, 1.0
	s_cbranch_scc0 .LBB0_1017
	v_cndmask_b32_e64 v166, 0, 1, s[24:25]
	v_cmp_ne_u32_e64 s[2:3], 1, v166
	s_andn2_b64 vcc, exec, s[24:25]
	s_cbranch_vccz .LBB0_1018

.LBB0_1029:
	s_andn2_b64 vcc, exec, s[10:11]
	s_cbranch_vccnz .LBB0_977
	s_branch .LBB0_977
.LBB0_1031:
	s_waitcnt vmcnt(0)
	s_andn2_b64 vcc, exec, s[12:13]
	s_cbranch_vccnz .Lbr_noextra
	s_barrier
.Lbr_noextra:
	s_barrier
.LBB0_1032:
	s_load_dwordx8 s[48:55], s[92:93], 0x110
	s_add_i32 s40, s79, 6
	s_mov_b32 s83, s79
	s_waitcnt lgkmcnt(0)
	s_mov_b32 s0, s54
	s_cmp_gt_i32 s0, s40
	s_cbranch_scc1 .LBB0_1114
	s_mov_b32 s0, s55
	s_cmp_ge_i32 s40, s0
	s_cbranch_scc1 .LBB0_1114
	v_readlane_b32 s0, v252, 16
	s_mov_b32 s1, -1
	v_readlane_b32 s41, v252, 2
	s_waitcnt vmcnt(0)
	v_mbcnt_lo_u32_b32 v0, s1, 0
	v_mbcnt_hi_u32_b32 v8, s1, v0
	v_lshl_add_u32 v9, s0, 6, v8
	v_readlane_b32 s0, v252, 4
	v_readlane_b32 s42, v252, 3
	s_ashr_i32 s43, s42, 31
	s_cmpk_lt_i32 s42, 0x200
	v_readlane_b32 s6, v253, 42
	s_mov_b64 s[0:1], s[92:93]
	s_cselect_b64 s[2:3], -1, 0
	s_cmpk_gt_i32 s42, 0x1ff
	v_readfirstlane_b32 s8, v9
	s_cbranch_scc1 .LBB0_1040
	s_lshr_b32 s4, s43, 29
	s_add_i32 s7, s42, s4
	s_and_b32 s4, s7, -8
	s_sub_i32 s9, s42, s4
	s_cmp_gt_i32 s9, -1
	s_mov_b64 s[4:5], -1
	s_cbranch_scc0 .LBB0_1037
	s_lshl_b32 s10, s9, 6
	s_mov_b64 s[4:5], 0
